# stack12 + bf16 GEMM units: the first two counted waits of a unit's first K-iteration no longer wait for the previous unit's epilogue store acknowledgements
# speedup vs baseline: 1.0035x; 1.0035x over previous
; #define LAS __attribute__((address_space(3)))
; __device__ __forceinline__ int fresh_lane() { unsigned z = 0u; asm volatile("" : "+v"(z)); return (int)__builtin_amdgcn_mbcnt_hi(~0u, __builtin_amdgcn_mbcnt_lo(~0u, z)); }
; __device__ __forceinline__ void ph1(const Ctx& c) {
;     const P& p = *c.pp;
;     pg8::RowOrder S; S.init(T, INW, c.G, c.bx, p.ws + WS_MIXED, p.ws + WS_WIN);
;     pg8::EpiQKV E{c.pp};
;     { const int t = c.wave * 64 + fresh_lane(); LAS float* tab = (LAS float*)(c.lds + TAB_EPI);
;       if (t < 336) tab[t] = t < 64 ? p.g_q_swa[t] : t < 128 ? p.g_k_swa[t - 64] : t < 160 ? p.g_q_diff[t - 128] : t < 192 ? p.g_k_diff[t - 160] : ((const float*)(p.ws + WS_ROT))[t - 192];
;       __syncthreads(); }
.LBB7_189:
	s_mov_b32 s99, 0
	v_readlane_b32 s4, v254, 2
	s_cmp_lt_i32 s4, 2
	s_cselect_b64 s[6:7], -1, 0
	s_and_b64 s[0:1], s[6:7], s[0:1]
	s_andn2_b64 vcc, exec, s[0:1]
	v_readlane_b32 s5, v254, 3
	s_cbranch_vccnz .LBB7_334
	v_mov_b32_e32 v0, 0
	v_readlane_b32 s0, v254, 5
	v_mbcnt_lo_u32_b32 v0, -1, v0
	v_mbcnt_hi_u32_b32 v0, -1, v0
	v_add_u32_e32 v0, s0, v0
	s_movk_i32 s0, 0x150
	v_cmp_gt_i32_e32 vcc, s0, v0
	s_and_saveexec_b64 s[0:1], vcc
	s_cbranch_execz .LBB7_208
	v_cmp_lt_i32_e32 vcc, 63, v0
	s_and_saveexec_b64 s[4:5], vcc
	s_xor_b64 s[4:5], exec, s[4:5]
	s_cbranch_execz .LBB7_205
	s_movk_i32 s2, 0x7f
	v_cmp_lt_u32_e32 vcc, s2, v0
	s_and_saveexec_b64 s[8:9], vcc
	s_xor_b64 s[8:9], exec, s[8:9]
	s_cbranch_execz .LBB7_202
	s_movk_i32 s2, 0x9f
	v_cmp_lt_u32_e32 vcc, s2, v0
	s_and_saveexec_b64 s[10:11], vcc
	s_xor_b64 s[10:11], exec, s[10:11]
	s_cbranch_execz .LBB7_199
	s_movk_i32 s2, 0xbf
	v_cmp_lt_u32_e32 vcc, s2, v0
	v_mov_b32_e32 v1, 0
	s_and_saveexec_b64 s[12:13], vcc
	s_xor_b64 s[12:13], exec, s[12:13]
	v_lshl_add_u64 v[2:3], v[0:1], 2, s[30:31]
	s_mov_b64 s[14:15], 0x39fd00
	v_lshl_add_u64 v[2:3], v[2:3], 0, s[14:15]
	s_andn2_saveexec_b64 s[12:13], s[12:13]
	s_cbranch_execz .LBB7_198
	v_readlane_b32 s36, v254, 9
	v_readlane_b32 s50, v254, 23
	v_readlane_b32 s51, v254, 24
	s_movk_i32 s14, 0xfd80
	s_mov_b32 s15, -1
	v_lshl_add_u64 v[2:3], v[0:1], 2, s[50:51]
	v_lshl_add_u64 v[2:3], v[2:3], 0, s[14:15]
	v_readlane_b32 s37, v254, 10
	v_readlane_b32 s38, v254, 11
	v_readlane_b32 s39, v254, 12
	v_readlane_b32 s40, v254, 13
	v_readlane_b32 s41, v254, 14
	v_readlane_b32 s42, v254, 15
	v_readlane_b32 s43, v254, 16
	v_readlane_b32 s44, v254, 17
	v_readlane_b32 s45, v254, 18
	v_readlane_b32 s46, v254, 19
	v_readlane_b32 s47, v254, 20
	v_readlane_b32 s48, v254, 21
	v_readlane_b32 s49, v254, 22

; #define PG8_STAGE_B(bufoff, gbase) PG8_STAGE2S(bufoff, gbase, voffB[0])
; #define PG8_STAGE_A(bufoff, gbase, off, h) do { if constexpr (Sched::GATHERS) PG8_STAGE2(bufoff, gbase, off[h][0], off[h][1]); \
;         else PG8_STAGE2S(bufoff, (const char*)(gbase) + (h) * hstep, voffA0); } while (0)
; #define PG8_LDA(dst, b, h) do { _Pragma("unroll") for (int m = 0; m < 4; ++m) { const v4i_t lo_ = *(const LAS v4i_t*)(lds + PG8_SA(b, h) + aoff + m * 2048), hi_ = *(const LAS v4i_t*)(lds + PG8_SA(b, h) + aoff + m * 2048 + 1024); \
;         dst[m] = __builtin_shufflevector(lo_, hi_, 0, 1, 2, 3, 4, 5, 6, 7); } } while (0)
; #define PG8_LDB(dst, b, h) do { _Pragma("unroll") for (int n = 0; n < 2; ++n) { const v4i_t lo_ = *(const LAS v4i_t*)(lds + PG8_SB(b, h) + boff + n * 2048), hi_ = *(const LAS v4i_t*)(lds + PG8_SB(b, h) + boff + n * 2048 + 1024); \
;         dst[n] = __builtin_shufflevector(lo_, hi_, 0, 1, 2, 3, 4, 5, 6, 7); } } while (0)
; #define PG8_WAIT_V(n) asm volatile("s_waitcnt vmcnt(" #n ")" ::: "memory")
; #define PG8_WAIT_L(n) asm volatile("s_waitcnt lgkmcnt(" #n ")" ::: "memory")
; #define PG8_BAR __builtin_amdgcn_s_barrier()
; #define PG8_SCHED __builtin_amdgcn_sched_barrier(0)
; template <class Epi, class Sched>
; __device__ __forceinline__ void gemm_phase(LAS unsigned char* lds, const Sched& S, const Epi& E, const int wid) {
;     ...
;             PG8_LDB(B0, 0, 0); PG8_LDB(B1, 0, 1); PG8_SCHED; PG8_LDA(At, 0, 0); PG8_STAGE_A(PG8_SA(1, 1), a1, gc, 1);
;             PG8_WAIT_V(8); PG8_WAIT_L(0); PG8_BAR; PG8_MMA(0, 0, At, B0); PG8_MMA(0, 1, At, B1); PG8_BAR; PG8_SCHED;
;             PG8_LDA(At, 0, 1); PG8_STAGE_B(PG8_SB(0, 0), b2); PG8_STAGE_B(PG8_SB(0, 1), b2 + hstep); PG8_STAGE_A(PG8_SA(0, 0), a2, o2, 0);
;             PG8_WAIT_V(8); PG8_WAIT_L(0); PG8_BAR; PG8_MMA(1, 0, At, B0); PG8_MMA(1, 1, At, B1); PG8_BAR; PG8_SCHED;
.LBB7_219:
	ds_read_b128 v[128:131], v192
	ds_read_b128 v[132:135], v192 offset:1024
	ds_read_b128 v[136:139], v192 offset:2048
	ds_read_b128 v[140:143], v192 offset:3072
	ds_read_b128 v[144:147], v193
	ds_read_b128 v[148:151], v193 offset:1024
	ds_read_b128 v[152:155], v193 offset:2048
	ds_read_b128 v[156:159], v193 offset:3072
	s_add_u32 s46, s44, 0x100
	s_addc_u32 s47, s45, 0
	s_cmp_eq_u32 s75, 12
	s_cselect_b32 s48, s36, s46
	s_cselect_b32 s49, s5, s47
	s_cselect_b32 s64, s37, s39
	s_cselect_b32 s65, s17, s74
	s_add_u32 s50, s48, 0x80
	s_addc_u32 s51, s49, 0
	ds_read_b128 v[160:163], v194
	ds_read_b128 v[164:167], v194 offset:1024
	ds_read_b128 v[174:177], v194 offset:2048
	ds_read_b128 v[178:181], v194 offset:3072
	ds_read_b128 v[182:185], v194 offset:4096
	ds_read_b128 v[186:189], v194 offset:5120
	ds_read_b128 v[200:203], v194 offset:6144
	ds_read_b128 v[204:207], v194 offset:7168
	s_add_u32 s76, s44, 0x40080
	s_addc_u32 s77, s45, 0
	s_mov_b32 s78, m0
	s_mov_b32 m0, s68
	s_nop 0
	global_load_lds_dwordx4 v191, s[76:77]
	s_mov_b32 m0, s78
	s_add_u32 s44, s44, 0x60080
	s_addc_u32 s45, s45, 0
	s_mov_b32 s76, m0
	s_mov_b32 m0, s69
	s_nop 0
	global_load_lds_dwordx4 v191, s[44:45]
	s_mov_b32 m0, s76
	s_cmp_eq_u32 s99, 1
	s_cbranch_scc1 .Lack1_0f
	s_waitcnt vmcnt(8)
	s_branch .Lack1_0d
.Lack1_0f:
	s_waitcnt vmcnt(18)
.Lack1_0d:
	s_waitcnt lgkmcnt(0)
	s_barrier
	s_setprio 1
	s_waitcnt lgkmcnt(7)
	v_mfma_f32_16x16x32_bf16 v[124:127], v[128:131], v[160:163], v[124:127]
	v_mfma_f32_16x16x32_bf16 v[120:123], v[136:139], v[160:163], v[120:123]
	s_waitcnt lgkmcnt(5)
	v_mfma_f32_16x16x32_bf16 v[108:111], v[128:131], v[174:177], v[108:111]
	v_mfma_f32_16x16x32_bf16 v[104:107], v[136:139], v[174:177], v[104:107]
	s_waitcnt lgkmcnt(3)
	v_mfma_f32_16x16x32_bf16 v[92:95], v[128:131], v[182:185], v[92:95]
	v_mfma_f32_16x16x32_bf16 v[88:91], v[136:139], v[182:185], v[88:91]
	s_waitcnt lgkmcnt(1)
	v_mfma_f32_16x16x32_bf16 v[76:79], v[128:131], v[200:203], v[76:79]
	v_mfma_f32_16x16x32_bf16 v[72:75], v[136:139], v[200:203], v[72:75]
	v_mfma_f32_16x16x32_bf16 v[124:127], v[132:135], v[164:167], v[124:127]
	v_mfma_f32_16x16x32_bf16 v[120:123], v[140:143], v[164:167], v[120:123]
	v_mfma_f32_16x16x32_bf16 v[108:111], v[132:135], v[178:181], v[108:111]
	v_mfma_f32_16x16x32_bf16 v[104:107], v[140:143], v[178:181], v[104:107]
	v_mfma_f32_16x16x32_bf16 v[92:95], v[132:135], v[186:189], v[92:95]
	v_mfma_f32_16x16x32_bf16 v[88:91], v[140:143], v[186:189], v[88:91]
	s_waitcnt lgkmcnt(0)
	v_mfma_f32_16x16x32_bf16 v[76:79], v[132:135], v[204:207], v[76:79]
	v_mfma_f32_16x16x32_bf16 v[72:75], v[140:143], v[204:207], v[72:75]
	s_setprio 0
	s_setprio 1
	v_mfma_f32_16x16x32_bf16 v[116:119], v[144:147], v[160:163], v[116:119]
	v_mfma_f32_16x16x32_bf16 v[112:115], v[152:155], v[160:163], v[112:115]
	v_mfma_f32_16x16x32_bf16 v[100:103], v[144:147], v[174:177], v[100:103]
	v_mfma_f32_16x16x32_bf16 v[96:99], v[152:155], v[174:177], v[96:99]
	v_mfma_f32_16x16x32_bf16 v[84:87], v[144:147], v[182:185], v[84:87]
	v_mfma_f32_16x16x32_bf16 v[80:83], v[152:155], v[182:185], v[80:83]
	v_mfma_f32_16x16x32_bf16 v[68:71], v[144:147], v[200:203], v[68:71]
	v_mfma_f32_16x16x32_bf16 v[64:67], v[152:155], v[200:203], v[64:67]
	v_mfma_f32_16x16x32_bf16 v[116:119], v[148:151], v[164:167], v[116:119]
	v_mfma_f32_16x16x32_bf16 v[112:115], v[156:159], v[164:167], v[112:115]
	v_mfma_f32_16x16x32_bf16 v[100:103], v[148:151], v[178:181], v[100:103]
	v_mfma_f32_16x16x32_bf16 v[96:99], v[156:159], v[178:181], v[96:99]
	v_mfma_f32_16x16x32_bf16 v[84:87], v[148:151], v[186:189], v[84:87]
	v_mfma_f32_16x16x32_bf16 v[80:83], v[156:159], v[186:189], v[80:83]
	v_mfma_f32_16x16x32_bf16 v[68:71], v[148:151], v[204:207], v[68:71]
	v_mfma_f32_16x16x32_bf16 v[64:67], v[156:159], v[204:207], v[64:67]
	s_setprio 0
	s_barrier
	ds_read_b128 v[160:163], v194 offset:16384
	ds_read_b128 v[164:167], v194 offset:17408
	ds_read_b128 v[174:177], v194 offset:18432
	ds_read_b128 v[178:181], v194 offset:19456
	ds_read_b128 v[182:185], v194 offset:20480
	ds_read_b128 v[186:189], v194 offset:21504
	ds_read_b128 v[200:203], v194 offset:22528
	ds_read_b128 v[204:207], v194 offset:23552
	s_mov_b32 s44, m0
	s_mov_b32 m0, s35
	s_nop 0
	global_load_lds_dwordx4 v190, s[64:65]
	s_mov_b32 m0, s44
	s_add_u32 s44, s64, 0x20000
	s_addc_u32 s45, s65, 0
	s_mov_b32 s76, m0
	s_mov_b32 m0, s52
	s_nop 0
	global_load_lds_dwordx4 v190, s[44:45]
	s_mov_b32 m0, s76
	s_add_u32 s44, s64, 0x40000
	s_addc_u32 s45, s65, 0
	s_mov_b32 s76, m0
	s_mov_b32 m0, s53
	s_nop 0
	global_load_lds_dwordx4 v190, s[44:45]
	s_mov_b32 m0, s76
	s_add_u32 s44, s64, 0x60000
	s_addc_u32 s45, s65, 0
	s_mov_b32 s76, m0
	s_mov_b32 m0, s54
	s_nop 0
	global_load_lds_dwordx4 v190, s[44:45]
	s_mov_b32 m0, s76
	s_mov_b32 s44, m0
	s_mov_b32 m0, s34
	s_nop 0
	global_load_lds_dwordx4 v191, s[48:49]
	s_mov_b32 m0, s44
	s_add_u32 s44, s48, 0x20000
	s_addc_u32 s45, s49, 0
	s_mov_b32 s76, m0
	s_mov_b32 m0, s55
	s_nop 0
	global_load_lds_dwordx4 v191, s[44:45]
	s_mov_b32 m0, s76
	s_cmp_eq_u32 s99, 1
	s_cbranch_scc1 .Lack1_1f
	s_waitcnt vmcnt(8)
	s_branch .Lack1_1d

; #define PG8_STAGE_A(bufoff, gbase, off, h) do { if constexpr (Sched::GATHERS) PG8_STAGE2(bufoff, gbase, off[h][0], off[h][1]); \
;         else PG8_STAGE2S(bufoff, (const char*)(gbase) + (h) * hstep, voffA0); } while (0)
; #define PG8_LDA(dst, b, h) do { _Pragma("unroll") for (int m = 0; m < 4; ++m) { const v4i_t lo_ = *(const LAS v4i_t*)(lds + PG8_SA(b, h) + aoff + m * 2048), hi_ = *(const LAS v4i_t*)(lds + PG8_SA(b, h) + aoff + m * 2048 + 1024); \
;         dst[m] = __builtin_shufflevector(lo_, hi_, 0, 1, 2, 3, 4, 5, 6, 7); } } while (0)
; #define PG8_LDB(dst, b, h) do { _Pragma("unroll") for (int n = 0; n < 2; ++n) { const v4i_t lo_ = *(const LAS v4i_t*)(lds + PG8_SB(b, h) + boff + n * 2048), hi_ = *(const LAS v4i_t*)(lds + PG8_SB(b, h) + boff + n * 2048 + 1024); \
;         dst[n] = __builtin_shufflevector(lo_, hi_, 0, 1, 2, 3, 4, 5, 6, 7); } } while (0)
; #define PG8_WAIT_V(n) asm volatile("s_waitcnt vmcnt(" #n ")" ::: "memory")
; #define PG8_WAIT_L(n) asm volatile("s_waitcnt lgkmcnt(" #n ")" ::: "memory")
; #define PG8_BAR __builtin_amdgcn_s_barrier()
; #define PG8_SCHED __builtin_amdgcn_sched_barrier(0)
; template <class Epi, class Sched>
; __device__ __forceinline__ void gemm_phase(LAS unsigned char* lds, const Sched& S, const Epi& E, const int wid) {
;     ...
;             PG8_WAIT_V(8); PG8_WAIT_L(0); PG8_BAR; PG8_MMA(1, 0, At, B0); PG8_MMA(1, 1, At, B1); PG8_BAR; PG8_SCHED;
;             PG8_LDB(B0, 1, 0); PG8_LDB(B1, 1, 1); PG8_SCHED; PG8_LDA(At, 1, 0); PG8_STAGE_A(PG8_SA(0, 1), a2, o2, 1);
;             PG8_WAIT_V(8); PG8_WAIT_L(0); PG8_BAR; PG8_MMA(0, 0, At, B0); PG8_MMA(0, 1, At, B1); PG8_BAR; PG8_SCHED;
.Lack1_1d:
	s_mov_b32 s99, 0
	s_waitcnt lgkmcnt(0)
	s_barrier
	s_setprio 1
	s_waitcnt lgkmcnt(7)
	v_mfma_f32_16x16x32_bf16 v[60:63], v[128:131], v[160:163], v[60:63]
	v_mfma_f32_16x16x32_bf16 v[56:59], v[136:139], v[160:163], v[56:59]
	s_waitcnt lgkmcnt(5)
	v_mfma_f32_16x16x32_bf16 v[44:47], v[128:131], v[174:177], v[44:47]
	v_mfma_f32_16x16x32_bf16 v[40:43], v[136:139], v[174:177], v[40:43]
	s_waitcnt lgkmcnt(3)
	v_mfma_f32_16x16x32_bf16 v[28:31], v[128:131], v[182:185], v[28:31]
	v_mfma_f32_16x16x32_bf16 v[24:27], v[136:139], v[182:185], v[24:27]
	s_waitcnt lgkmcnt(1)
	v_mfma_f32_16x16x32_bf16 v[12:15], v[128:131], v[200:203], v[12:15]
	v_mfma_f32_16x16x32_bf16 v[8:11], v[136:139], v[200:203], v[8:11]
	v_mfma_f32_16x16x32_bf16 v[60:63], v[132:135], v[164:167], v[60:63]
	v_mfma_f32_16x16x32_bf16 v[56:59], v[140:143], v[164:167], v[56:59]
	v_mfma_f32_16x16x32_bf16 v[44:47], v[132:135], v[178:181], v[44:47]
	v_mfma_f32_16x16x32_bf16 v[40:43], v[140:143], v[178:181], v[40:43]
	v_mfma_f32_16x16x32_bf16 v[28:31], v[132:135], v[186:189], v[28:31]
	v_mfma_f32_16x16x32_bf16 v[24:27], v[140:143], v[186:189], v[24:27]
	s_waitcnt lgkmcnt(0)
	v_mfma_f32_16x16x32_bf16 v[12:15], v[132:135], v[204:207], v[12:15]
	v_mfma_f32_16x16x32_bf16 v[8:11], v[140:143], v[204:207], v[8:11]
	s_setprio 0
	s_setprio 1
	v_mfma_f32_16x16x32_bf16 v[52:55], v[144:147], v[160:163], v[52:55]
	v_mfma_f32_16x16x32_bf16 v[48:51], v[152:155], v[160:163], v[48:51]
	v_mfma_f32_16x16x32_bf16 v[36:39], v[144:147], v[174:177], v[36:39]
	v_mfma_f32_16x16x32_bf16 v[32:35], v[152:155], v[174:177], v[32:35]
	v_mfma_f32_16x16x32_bf16 v[20:23], v[144:147], v[182:185], v[20:23]
	v_mfma_f32_16x16x32_bf16 v[16:19], v[152:155], v[182:185], v[16:19]
	v_mfma_f32_16x16x32_bf16 v[4:7], v[144:147], v[200:203], v[4:7]
	v_mfma_f32_16x16x32_bf16 v[0:3], v[152:155], v[200:203], v[0:3]
	v_mfma_f32_16x16x32_bf16 v[52:55], v[148:151], v[164:167], v[52:55]
	v_mfma_f32_16x16x32_bf16 v[48:51], v[156:159], v[164:167], v[48:51]
	v_mfma_f32_16x16x32_bf16 v[36:39], v[148:151], v[178:181], v[36:39]
	v_mfma_f32_16x16x32_bf16 v[32:35], v[156:159], v[178:181], v[32:35]
	v_mfma_f32_16x16x32_bf16 v[20:23], v[148:151], v[186:189], v[20:23]
	v_mfma_f32_16x16x32_bf16 v[16:19], v[156:159], v[186:189], v[16:19]
	v_mfma_f32_16x16x32_bf16 v[4:7], v[148:151], v[204:207], v[4:7]
	v_mfma_f32_16x16x32_bf16 v[0:3], v[156:159], v[204:207], v[0:3]
	s_setprio 0
	s_barrier
	ds_read_b128 v[128:131], v195
	ds_read_b128 v[132:135], v195 offset:1024
	ds_read_b128 v[136:139], v195 offset:2048
	ds_read_b128 v[140:143], v195 offset:3072
	ds_read_b128 v[144:147], v196
	ds_read_b128 v[148:151], v196 offset:1024
	ds_read_b128 v[152:155], v196 offset:2048
	ds_read_b128 v[156:159], v196 offset:3072
	ds_read_b128 v[160:163], v194 offset:32768
	ds_read_b128 v[164:167], v194 offset:33792
	ds_read_b128 v[174:177], v194 offset:34816
	ds_read_b128 v[178:181], v194 offset:35840
	ds_read_b128 v[182:185], v194 offset:36864
	ds_read_b128 v[186:189], v194 offset:37888
	ds_read_b128 v[200:203], v194 offset:38912
	ds_read_b128 v[204:207], v194 offset:39936
	s_add_u32 s44, s48, 0x40000
	s_addc_u32 s45, s49, 0
	s_mov_b32 s76, m0
	s_mov_b32 m0, s56
	s_nop 0
	global_load_lds_dwordx4 v191, s[44:45]
	s_mov_b32 m0, s76
	s_add_u32 s44, s48, 0x60000
	s_addc_u32 s45, s49, 0
	s_mov_b32 s76, m0
	s_mov_b32 m0, s57
	s_nop 0
	global_load_lds_dwordx4 v191, s[44:45]
	s_mov_b32 m0, s76
	s_waitcnt vmcnt(8)
	s_waitcnt lgkmcnt(0)
	s_barrier
	s_setprio 1
	s_waitcnt lgkmcnt(7)
	v_mfma_f32_16x16x32_bf16 v[124:127], v[128:131], v[160:163], v[124:127]
	v_mfma_f32_16x16x32_bf16 v[120:123], v[136:139], v[160:163], v[120:123]
	s_waitcnt lgkmcnt(5)
	v_mfma_f32_16x16x32_bf16 v[108:111], v[128:131], v[174:177], v[108:111]
	v_mfma_f32_16x16x32_bf16 v[104:107], v[136:139], v[174:177], v[104:107]
	s_waitcnt lgkmcnt(3)
	v_mfma_f32_16x16x32_bf16 v[92:95], v[128:131], v[182:185], v[92:95]
	v_mfma_f32_16x16x32_bf16 v[88:91], v[136:139], v[182:185], v[88:91]
	s_waitcnt lgkmcnt(1)
	v_mfma_f32_16x16x32_bf16 v[76:79], v[128:131], v[200:203], v[76:79]
	v_mfma_f32_16x16x32_bf16 v[72:75], v[136:139], v[200:203], v[72:75]
	v_mfma_f32_16x16x32_bf16 v[124:127], v[132:135], v[164:167], v[124:127]
	v_mfma_f32_16x16x32_bf16 v[120:123], v[140:143], v[164:167], v[120:123]
	v_mfma_f32_16x16x32_bf16 v[108:111], v[132:135], v[178:181], v[108:111]
	v_mfma_f32_16x16x32_bf16 v[104:107], v[140:143], v[178:181], v[104:107]
	v_mfma_f32_16x16x32_bf16 v[92:95], v[132:135], v[186:189], v[92:95]
	v_mfma_f32_16x16x32_bf16 v[88:91], v[140:143], v[186:189], v[88:91]
	s_waitcnt lgkmcnt(0)
	v_mfma_f32_16x16x32_bf16 v[76:79], v[132:135], v[204:207], v[76:79]
	v_mfma_f32_16x16x32_bf16 v[72:75], v[140:143], v[204:207], v[72:75]
	s_setprio 0
	s_setprio 1
	v_mfma_f32_16x16x32_bf16 v[116:119], v[144:147], v[160:163], v[116:119]
	v_mfma_f32_16x16x32_bf16 v[112:115], v[152:155], v[160:163], v[112:115]
	v_mfma_f32_16x16x32_bf16 v[100:103], v[144:147], v[174:177], v[100:103]
	v_mfma_f32_16x16x32_bf16 v[96:99], v[152:155], v[174:177], v[96:99]
	v_mfma_f32_16x16x32_bf16 v[84:87], v[144:147], v[182:185], v[84:87]
	v_mfma_f32_16x16x32_bf16 v[80:83], v[152:155], v[182:185], v[80:83]
	v_mfma_f32_16x16x32_bf16 v[68:71], v[144:147], v[200:203], v[68:71]
	v_mfma_f32_16x16x32_bf16 v[64:67], v[152:155], v[200:203], v[64:67]
	v_mfma_f32_16x16x32_bf16 v[116:119], v[148:151], v[164:167], v[116:119]
	v_mfma_f32_16x16x32_bf16 v[112:115], v[156:159], v[164:167], v[112:115]
	v_mfma_f32_16x16x32_bf16 v[100:103], v[148:151], v[178:181], v[100:103]
	v_mfma_f32_16x16x32_bf16 v[96:99], v[156:159], v[178:181], v[96:99]
	v_mfma_f32_16x16x32_bf16 v[84:87], v[148:151], v[186:189], v[84:87]
	v_mfma_f32_16x16x32_bf16 v[80:83], v[156:159], v[186:189], v[80:83]
	v_mfma_f32_16x16x32_bf16 v[68:71], v[148:151], v[204:207], v[68:71]
	v_mfma_f32_16x16x32_bf16 v[64:67], v[156:159], v[204:207], v[64:67]
	s_setprio 0
	s_barrier
; #define PG8_STAGE_B(bufoff, gbase) PG8_STAGE2S(bufoff, gbase, voffB[0])
; #define PG8_STAGE_A(bufoff, gbase, off, h) do { if constexpr (Sched::GATHERS) PG8_STAGE2(bufoff, gbase, off[h][0], off[h][1]); \
;         else PG8_STAGE2S(bufoff, (const char*)(gbase) + (h) * hstep, voffA0); } while (0)
; #define PG8_LDA(dst, b, h) do { _Pragma("unroll") for (int m = 0; m < 4; ++m) { const v4i_t lo_ = *(const LAS v4i_t*)(lds + PG8_SA(b, h) + aoff + m * 2048), hi_ = *(const LAS v4i_t*)(lds + PG8_SA(b, h) + aoff + m * 2048 + 1024); \
;         dst[m] = __builtin_shufflevector(lo_, hi_, 0, 1, 2, 3, 4, 5, 6, 7); } } while (0)
; #define PG8_WAIT_V(n) asm volatile("s_waitcnt vmcnt(" #n ")" ::: "memory")
; #define PG8_WAIT_L(n) asm volatile("s_waitcnt lgkmcnt(" #n ")" ::: "memory")
; #define PG8_BAR __builtin_amdgcn_s_barrier()
; #define PG8_SCHED __builtin_amdgcn_sched_barrier(0)
; template <class Epi, class Sched>
; __device__ __forceinline__ void gemm_phase(LAS unsigned char* lds, const Sched& S, const Epi& E, const int wid) {
;     ...
;             PG8_LDA(At, 1, 1); PG8_STAGE_B(PG8_SB(1, 0), b3); PG8_STAGE_B(PG8_SB(1, 1), b3 + hstep); PG8_STAGE_A(PG8_SA(1, 0), a3, o2, 0);
;             PG8_WAIT_V(8); PG8_WAIT_L(0); PG8_BAR; PG8_MMA(1, 0, At, B0); PG8_MMA(1, 1, At, B1); PG8_BAR; PG8_SCHED;
;         }
;         if (wr == 0) PG8_BAR;
	s_add_u32 s44, s64, 0x80
	s_addc_u32 s45, s65, 0
	ds_read_b128 v[160:163], v194 offset:49152
	ds_read_b128 v[164:167], v194 offset:50176
	ds_read_b128 v[174:177], v194 offset:51200
	ds_read_b128 v[178:181], v194 offset:52224
	ds_read_b128 v[182:185], v194 offset:53248
	ds_read_b128 v[186:189], v194 offset:54272
	ds_read_b128 v[200:203], v194 offset:55296
	ds_read_b128 v[204:207], v194 offset:56320
	s_mov_b32 s76, m0
	s_mov_b32 m0, s60
	s_nop 0
	global_load_lds_dwordx4 v190, s[44:45]
	s_mov_b32 m0, s76
	s_add_u32 s44, s64, 0x20080
	s_addc_u32 s45, s65, 0
	s_mov_b32 s76, m0
	s_mov_b32 m0, s61
	s_nop 0
	global_load_lds_dwordx4 v190, s[44:45]
	s_mov_b32 m0, s76
	s_add_u32 s44, s64, 0x40080
	s_addc_u32 s45, s65, 0
	s_mov_b32 s76, m0
	s_mov_b32 m0, s66
	s_nop 0
	global_load_lds_dwordx4 v190, s[44:45]
	s_mov_b32 m0, s76
	s_add_u32 s44, s64, 0x60080
	s_addc_u32 s45, s65, 0
	s_mov_b32 s64, m0
	s_mov_b32 m0, s67
	s_nop 0
	global_load_lds_dwordx4 v190, s[44:45]
	s_mov_b32 m0, s64
	s_mov_b32 s44, m0
	s_mov_b32 m0, s62
	s_nop 0
	global_load_lds_dwordx4 v191, s[50:51]
	s_mov_b32 m0, s44
	s_add_u32 s44, s48, 0x20080
	s_addc_u32 s45, s49, 0
	s_mov_b32 s48, m0
	s_mov_b32 m0, s63
	s_nop 0
	global_load_lds_dwordx4 v191, s[44:45]
	s_mov_b32 m0, s48
	s_waitcnt vmcnt(8)
	s_waitcnt lgkmcnt(0)
	s_barrier
	s_setprio 1
	s_waitcnt lgkmcnt(7)
	v_mfma_f32_16x16x32_bf16 v[60:63], v[128:131], v[160:163], v[60:63]
	v_mfma_f32_16x16x32_bf16 v[56:59], v[136:139], v[160:163], v[56:59]
	s_waitcnt lgkmcnt(5)
	v_mfma_f32_16x16x32_bf16 v[44:47], v[128:131], v[174:177], v[44:47]
	v_mfma_f32_16x16x32_bf16 v[40:43], v[136:139], v[174:177], v[40:43]
	s_waitcnt lgkmcnt(3)
	v_mfma_f32_16x16x32_bf16 v[28:31], v[128:131], v[182:185], v[28:31]
	v_mfma_f32_16x16x32_bf16 v[24:27], v[136:139], v[182:185], v[24:27]
	s_waitcnt lgkmcnt(1)
	v_mfma_f32_16x16x32_bf16 v[12:15], v[128:131], v[200:203], v[12:15]
	v_mfma_f32_16x16x32_bf16 v[8:11], v[136:139], v[200:203], v[8:11]
	v_mfma_f32_16x16x32_bf16 v[60:63], v[132:135], v[164:167], v[60:63]
	v_mfma_f32_16x16x32_bf16 v[56:59], v[140:143], v[164:167], v[56:59]
	v_mfma_f32_16x16x32_bf16 v[44:47], v[132:135], v[178:181], v[44:47]
	v_mfma_f32_16x16x32_bf16 v[40:43], v[140:143], v[178:181], v[40:43]
	v_mfma_f32_16x16x32_bf16 v[28:31], v[132:135], v[186:189], v[28:31]
	v_mfma_f32_16x16x32_bf16 v[24:27], v[140:143], v[186:189], v[24:27]
	s_waitcnt lgkmcnt(0)
	v_mfma_f32_16x16x32_bf16 v[12:15], v[132:135], v[204:207], v[12:15]
	v_mfma_f32_16x16x32_bf16 v[8:11], v[140:143], v[204:207], v[8:11]
	s_setprio 0
	s_setprio 1
	v_mfma_f32_16x16x32_bf16 v[52:55], v[144:147], v[160:163], v[52:55]
	v_mfma_f32_16x16x32_bf16 v[48:51], v[152:155], v[160:163], v[48:51]
	v_mfma_f32_16x16x32_bf16 v[36:39], v[144:147], v[174:177], v[36:39]
	v_mfma_f32_16x16x32_bf16 v[32:35], v[152:155], v[174:177], v[32:35]
	v_mfma_f32_16x16x32_bf16 v[20:23], v[144:147], v[182:185], v[20:23]
	v_mfma_f32_16x16x32_bf16 v[16:19], v[152:155], v[182:185], v[16:19]
	v_mfma_f32_16x16x32_bf16 v[4:7], v[144:147], v[200:203], v[4:7]
	v_mfma_f32_16x16x32_bf16 v[0:3], v[152:155], v[200:203], v[0:3]
	v_mfma_f32_16x16x32_bf16 v[52:55], v[148:151], v[164:167], v[52:55]
	v_mfma_f32_16x16x32_bf16 v[48:51], v[156:159], v[164:167], v[48:51]
	v_mfma_f32_16x16x32_bf16 v[36:39], v[148:151], v[178:181], v[36:39]
	v_mfma_f32_16x16x32_bf16 v[32:35], v[156:159], v[178:181], v[32:35]
	v_mfma_f32_16x16x32_bf16 v[20:23], v[148:151], v[186:189], v[20:23]
	v_mfma_f32_16x16x32_bf16 v[16:19], v[156:159], v[186:189], v[16:19]
	v_mfma_f32_16x16x32_bf16 v[4:7], v[148:151], v[204:207], v[4:7]
	v_mfma_f32_16x16x32_bf16 v[0:3], v[156:159], v[204:207], v[0:3]
	s_setprio 0
	s_barrier
	s_add_i32 s75, s75, 2
	s_add_u32 s39, s39, 0x100
	s_addc_u32 s74, s74, 0
	s_cmp_gt_u32 s75, 13
	s_mov_b64 s[44:45], s[46:47]
	s_cbranch_scc0 .LBB7_219
	s_mov_b32 s99, 1
	s_and_b64 vcc, exec, s[12:13]
	s_cbranch_vccz .LBB7_222
	s_barrier

;     __device__ __forceinline__ bool next(int i, Unit& u) const {
;         const long L = (long)i * G + c; if (L >= nwg) return false;
;         int wgid = (int)L; { const int q = nwg / NXCD, r = nwg % NXCD, xcd = wgid % NXCD, off = wgid / NXCD; wgid = (xcd < r ? xcd * (q + 1) : r * (q + 1) + (xcd - r) * q) + off; }
;         const int nig = WGM * nN, gid = wgid / nig, fm = gid * WGM, gsz = (nM - fm) < WGM ? (nM - fm) : WGM;
;         u.pm = fm + ((wgid % nig) % gsz); u.pn = (wgid % nig) / gsz; u.e = 0; u.pos0 = 0; u.cnt = 0; return true;
; __device__ __forceinline__ void ph3(const Ctx& c) {
;     const P& p = *c.pp;
;     pg8::RowOrder S; S.init(T, DM, c.G, c.bx, p.ws + WS_MIXED, p.ws + WS_WOUT);
;     pg8::EpiO E{(bf16_t*)p.out};
;     pg8::gemm_phase<pg8::EpiO, pg8::RowOrder>(c.lds + RING_OFF, S, E, c.wave);
.LBB7_609:
	s_mov_b32 s99, 0
	v_readlane_b32 s4, v254, 2
	v_readlane_b32 s5, v254, 3
	s_cmp_lt_i32 s4, 4
	s_cselect_b64 s[4:5], -1, 0
	s_and_b64 s[0:1], s[4:5], s[0:1]
	s_andn2_b64 vcc, exec, s[0:1]
	s_cbranch_vccnz .LBB7_634
	s_waitcnt vmcnt(0)
	v_mov_b32_e32 v0, 0
	s_cmpk_gt_i32 s92, 0x3ff
	s_cbranch_scc1 .LBB7_634
	s_ashr_i32 s2, s92, 31
	s_lshr_b32 s0, s2, 29
	s_add_i32 s8, s92, s0
	s_and_b32 s0, s8, -8
	s_sub_i32 s7, s92, s0
	s_cmp_gt_i32 s7, -1
	s_cbranch_scc0 .LBB7_613
	s_lshl_b32 s6, s7, 7
	s_ashr_i32 s0, s8, 3
	s_cbranch_execz .LBB7_614
	s_branch .LBB7_615

; #define PG8_STAGE_A(bufoff, gbase, off, h) do { if constexpr (Sched::GATHERS) PG8_STAGE2(bufoff, gbase, off[h][0], off[h][1]); \
;         else PG8_STAGE2S(bufoff, (const char*)(gbase) + (h) * hstep, voffA0); } while (0)
; #define PG8_LDA(dst, b, h) do { _Pragma("unroll") for (int m = 0; m < 4; ++m) { const v4i_t lo_ = *(const LAS v4i_t*)(lds + PG8_SA(b, h) + aoff + m * 2048), hi_ = *(const LAS v4i_t*)(lds + PG8_SA(b, h) + aoff + m * 2048 + 1024); \
;         dst[m] = __builtin_shufflevector(lo_, hi_, 0, 1, 2, 3, 4, 5, 6, 7); } } while (0)
; #define PG8_LDB(dst, b, h) do { _Pragma("unroll") for (int n = 0; n < 2; ++n) { const v4i_t lo_ = *(const LAS v4i_t*)(lds + PG8_SB(b, h) + boff + n * 2048), hi_ = *(const LAS v4i_t*)(lds + PG8_SB(b, h) + boff + n * 2048 + 1024); \
;         dst[n] = __builtin_shufflevector(lo_, hi_, 0, 1, 2, 3, 4, 5, 6, 7); } } while (0)
; #define PG8_WAIT_V(n) asm volatile("s_waitcnt vmcnt(" #n ")" ::: "memory")
; #define PG8_WAIT_L(n) asm volatile("s_waitcnt lgkmcnt(" #n ")" ::: "memory")
; #define PG8_BAR __builtin_amdgcn_s_barrier()
; #define PG8_SCHED __builtin_amdgcn_sched_barrier(0)
; template <class Epi, class Sched>
; __device__ __forceinline__ void gemm_phase(LAS unsigned char* lds, const Sched& S, const Epi& E, const int wid) {
;     ...
;             PG8_LDB(B0, 0, 0); PG8_LDB(B1, 0, 1); PG8_SCHED; PG8_LDA(At, 0, 0); PG8_STAGE_A(PG8_SA(1, 1), a1, gc, 1);
;             PG8_WAIT_V(8); PG8_WAIT_L(0); PG8_BAR; PG8_MMA(0, 0, At, B0); PG8_MMA(0, 1, At, B1); PG8_BAR; PG8_SCHED;
.LBB7_627:
	ds_read_b128 v[142:145], v136
	ds_read_b128 v[146:149], v136 offset:1024
	ds_read_b128 v[150:153], v136 offset:2048
	ds_read_b128 v[154:157], v136 offset:3072
	ds_read_b128 v[158:161], v137
	ds_read_b128 v[162:165], v137 offset:1024
	ds_read_b128 v[166:169], v137 offset:2048
	ds_read_b128 v[170:173], v137 offset:3072
	s_add_u32 s48, s46, 0x100
	s_addc_u32 s49, s47, 0
	s_cmp_eq_u32 s81, 12
	s_cselect_b32 s50, s77, s48
	s_cselect_b32 s51, s39, s49
	s_cselect_b32 s54, s78, s79
	s_cselect_b32 s55, s25, s80
	s_add_u32 s52, s50, 0x80
	s_addc_u32 s53, s51, 0
	ds_read_b128 v[174:177], v138
	ds_read_b128 v[178:181], v138 offset:1024
	ds_read_b128 v[182:185], v138 offset:2048
	ds_read_b128 v[186:189], v138 offset:3072
	ds_read_b128 v[190:193], v138 offset:4096
	ds_read_b128 v[194:197], v138 offset:5120
	ds_read_b128 v[198:201], v138 offset:6144
	ds_read_b128 v[202:205], v138 offset:7168
	s_add_u32 s82, s46, 0x40080
	s_addc_u32 s83, s47, 0
	s_mov_b32 s84, m0
	s_mov_b32 m0, s69
	s_nop 0
	global_load_lds_dwordx4 v135, s[82:83]
	s_mov_b32 m0, s84
	s_add_u32 s46, s46, 0x60080
	s_addc_u32 s47, s47, 0
	s_mov_b32 s82, m0
	s_mov_b32 m0, s70
	s_nop 0
	global_load_lds_dwordx4 v135, s[46:47]
	s_mov_b32 m0, s82
	s_cmp_eq_u32 s99, 1
	s_cbranch_scc1 .Lack3_0f
	s_waitcnt vmcnt(8)
	s_branch .Lack3_0d

; #define PG8_STAGE_B(bufoff, gbase) PG8_STAGE2S(bufoff, gbase, voffB[0])
; #define PG8_STAGE_A(bufoff, gbase, off, h) do { if constexpr (Sched::GATHERS) PG8_STAGE2(bufoff, gbase, off[h][0], off[h][1]); \
;         else PG8_STAGE2S(bufoff, (const char*)(gbase) + (h) * hstep, voffA0); } while (0)
; #define PG8_LDA(dst, b, h) do { _Pragma("unroll") for (int m = 0; m < 4; ++m) { const v4i_t lo_ = *(const LAS v4i_t*)(lds + PG8_SA(b, h) + aoff + m * 2048), hi_ = *(const LAS v4i_t*)(lds + PG8_SA(b, h) + aoff + m * 2048 + 1024); \
;         dst[m] = __builtin_shufflevector(lo_, hi_, 0, 1, 2, 3, 4, 5, 6, 7); } } while (0)
; #define PG8_WAIT_V(n) asm volatile("s_waitcnt vmcnt(" #n ")" ::: "memory")
; #define PG8_WAIT_L(n) asm volatile("s_waitcnt lgkmcnt(" #n ")" ::: "memory")
; #define PG8_BAR __builtin_amdgcn_s_barrier()
; #define PG8_SCHED __builtin_amdgcn_sched_barrier(0)
; template <class Epi, class Sched>
; __device__ __forceinline__ void gemm_phase(LAS unsigned char* lds, const Sched& S, const Epi& E, const int wid) {
;     ...
;             PG8_WAIT_V(8); PG8_WAIT_L(0); PG8_BAR; PG8_MMA(0, 0, At, B0); PG8_MMA(0, 1, At, B1); PG8_BAR; PG8_SCHED;
;             PG8_LDA(At, 0, 1); PG8_STAGE_B(PG8_SB(0, 0), b2); PG8_STAGE_B(PG8_SB(0, 1), b2 + hstep); PG8_STAGE_A(PG8_SA(0, 0), a2, o2, 0);
;             PG8_WAIT_V(8); PG8_WAIT_L(0); PG8_BAR; PG8_MMA(1, 0, At, B0); PG8_MMA(1, 1, At, B1); PG8_BAR; PG8_SCHED;
.Lack3_0d:
	s_waitcnt lgkmcnt(0)
	s_barrier
	s_setprio 1
	s_waitcnt lgkmcnt(7)
	v_mfma_f32_16x16x32_bf16 v[124:127], v[142:145], v[174:177], v[124:127]
	v_mfma_f32_16x16x32_bf16 v[120:123], v[150:153], v[174:177], v[120:123]
	s_waitcnt lgkmcnt(5)
	v_mfma_f32_16x16x32_bf16 v[116:119], v[142:145], v[182:185], v[116:119]
	v_mfma_f32_16x16x32_bf16 v[108:111], v[150:153], v[182:185], v[108:111]
	s_waitcnt lgkmcnt(3)
	v_mfma_f32_16x16x32_bf16 v[100:103], v[142:145], v[190:193], v[100:103]
	v_mfma_f32_16x16x32_bf16 v[92:95], v[150:153], v[190:193], v[92:95]
	s_waitcnt lgkmcnt(1)
	v_mfma_f32_16x16x32_bf16 v[84:87], v[142:145], v[198:201], v[84:87]
	v_mfma_f32_16x16x32_bf16 v[76:79], v[150:153], v[198:201], v[76:79]
	v_mfma_f32_16x16x32_bf16 v[124:127], v[146:149], v[178:181], v[124:127]
	v_mfma_f32_16x16x32_bf16 v[120:123], v[154:157], v[178:181], v[120:123]
	v_mfma_f32_16x16x32_bf16 v[116:119], v[146:149], v[186:189], v[116:119]
	v_mfma_f32_16x16x32_bf16 v[108:111], v[154:157], v[186:189], v[108:111]
	v_mfma_f32_16x16x32_bf16 v[100:103], v[146:149], v[194:197], v[100:103]
	v_mfma_f32_16x16x32_bf16 v[92:95], v[154:157], v[194:197], v[92:95]
	s_waitcnt lgkmcnt(0)
	v_mfma_f32_16x16x32_bf16 v[84:87], v[146:149], v[202:205], v[84:87]
	v_mfma_f32_16x16x32_bf16 v[76:79], v[154:157], v[202:205], v[76:79]
	s_setprio 0
	s_setprio 1
	v_mfma_f32_16x16x32_bf16 v[112:115], v[158:161], v[174:177], v[112:115]
	v_mfma_f32_16x16x32_bf16 v[104:107], v[166:169], v[174:177], v[104:107]
	v_mfma_f32_16x16x32_bf16 v[96:99], v[158:161], v[182:185], v[96:99]
	v_mfma_f32_16x16x32_bf16 v[88:91], v[166:169], v[182:185], v[88:91]
	v_mfma_f32_16x16x32_bf16 v[80:83], v[158:161], v[190:193], v[80:83]
	v_mfma_f32_16x16x32_bf16 v[72:75], v[166:169], v[190:193], v[72:75]
	v_mfma_f32_16x16x32_bf16 v[68:71], v[158:161], v[198:201], v[68:71]
	v_mfma_f32_16x16x32_bf16 v[64:67], v[166:169], v[198:201], v[64:67]
	v_mfma_f32_16x16x32_bf16 v[112:115], v[162:165], v[178:181], v[112:115]
	v_mfma_f32_16x16x32_bf16 v[104:107], v[170:173], v[178:181], v[104:107]
	v_mfma_f32_16x16x32_bf16 v[96:99], v[162:165], v[186:189], v[96:99]
	v_mfma_f32_16x16x32_bf16 v[88:91], v[170:173], v[186:189], v[88:91]
	v_mfma_f32_16x16x32_bf16 v[80:83], v[162:165], v[194:197], v[80:83]
	v_mfma_f32_16x16x32_bf16 v[72:75], v[170:173], v[194:197], v[72:75]
	v_mfma_f32_16x16x32_bf16 v[68:71], v[162:165], v[202:205], v[68:71]
	v_mfma_f32_16x16x32_bf16 v[64:67], v[170:173], v[202:205], v[64:67]
	s_setprio 0
	s_barrier
	ds_read_b128 v[174:177], v138 offset:16384
	ds_read_b128 v[178:181], v138 offset:17408
	ds_read_b128 v[182:185], v138 offset:18432
	ds_read_b128 v[186:189], v138 offset:19456
	ds_read_b128 v[190:193], v138 offset:20480
	ds_read_b128 v[194:197], v138 offset:21504
	ds_read_b128 v[198:201], v138 offset:22528
	ds_read_b128 v[202:205], v138 offset:23552
	s_mov_b32 s46, m0
	s_mov_b32 m0, s37
	s_nop 0
	global_load_lds_dwordx4 v134, s[54:55]
	s_mov_b32 m0, s46
	s_add_u32 s46, s54, 0x20000
	s_addc_u32 s47, s55, 0
	s_mov_b32 s82, m0
	s_mov_b32 m0, s45
	s_nop 0
	global_load_lds_dwordx4 v134, s[46:47]
	s_mov_b32 m0, s82
	s_add_u32 s46, s54, 0x40000
	s_addc_u32 s47, s55, 0
	s_mov_b32 s82, m0
	s_mov_b32 m0, s56
	s_nop 0
	global_load_lds_dwordx4 v134, s[46:47]
	s_mov_b32 m0, s82
	s_add_u32 s46, s54, 0x60000
	s_addc_u32 s47, s55, 0
	s_mov_b32 s82, m0
	s_mov_b32 m0, s57
	s_nop 0
	global_load_lds_dwordx4 v134, s[46:47]
	s_mov_b32 m0, s82
	s_mov_b32 s46, m0
	s_mov_b32 m0, s36
	s_nop 0
	global_load_lds_dwordx4 v135, s[50:51]
	s_mov_b32 m0, s46
	s_add_u32 s46, s50, 0x20000
	s_addc_u32 s47, s51, 0
	s_mov_b32 s82, m0
	s_mov_b32 m0, s58
	s_nop 0
	global_load_lds_dwordx4 v135, s[46:47]
	s_mov_b32 m0, s82
	s_cmp_eq_u32 s99, 1
	s_cbranch_scc1 .Lack3_1f
	s_waitcnt vmcnt(8)
	s_branch .Lack3_1d

; #define PG8_STAGE_A(bufoff, gbase, off, h) do { if constexpr (Sched::GATHERS) PG8_STAGE2(bufoff, gbase, off[h][0], off[h][1]); \
;         else PG8_STAGE2S(bufoff, (const char*)(gbase) + (h) * hstep, voffA0); } while (0)
; #define PG8_LDA(dst, b, h) do { _Pragma("unroll") for (int m = 0; m < 4; ++m) { const v4i_t lo_ = *(const LAS v4i_t*)(lds + PG8_SA(b, h) + aoff + m * 2048), hi_ = *(const LAS v4i_t*)(lds + PG8_SA(b, h) + aoff + m * 2048 + 1024); \
;         dst[m] = __builtin_shufflevector(lo_, hi_, 0, 1, 2, 3, 4, 5, 6, 7); } } while (0)
; #define PG8_LDB(dst, b, h) do { _Pragma("unroll") for (int n = 0; n < 2; ++n) { const v4i_t lo_ = *(const LAS v4i_t*)(lds + PG8_SB(b, h) + boff + n * 2048), hi_ = *(const LAS v4i_t*)(lds + PG8_SB(b, h) + boff + n * 2048 + 1024); \
;         dst[n] = __builtin_shufflevector(lo_, hi_, 0, 1, 2, 3, 4, 5, 6, 7); } } while (0)
; #define PG8_WAIT_V(n) asm volatile("s_waitcnt vmcnt(" #n ")" ::: "memory")
; #define PG8_WAIT_L(n) asm volatile("s_waitcnt lgkmcnt(" #n ")" ::: "memory")
; #define PG8_BAR __builtin_amdgcn_s_barrier()
; #define PG8_SCHED __builtin_amdgcn_sched_barrier(0)
; template <class Epi, class Sched>
; __device__ __forceinline__ void gemm_phase(LAS unsigned char* lds, const Sched& S, const Epi& E, const int wid) {
;     ...
;             PG8_WAIT_V(8); PG8_WAIT_L(0); PG8_BAR; PG8_MMA(1, 0, At, B0); PG8_MMA(1, 1, At, B1); PG8_BAR; PG8_SCHED;
;             PG8_LDB(B0, 1, 0); PG8_LDB(B1, 1, 1); PG8_SCHED; PG8_LDA(At, 1, 0); PG8_STAGE_A(PG8_SA(0, 1), a2, o2, 1);
;             PG8_WAIT_V(8); PG8_WAIT_L(0); PG8_BAR; PG8_MMA(0, 0, At, B0); PG8_MMA(0, 1, At, B1); PG8_BAR; PG8_SCHED;
.Lack3_1d:
	s_mov_b32 s99, 0
	s_waitcnt lgkmcnt(0)
	s_barrier
	s_setprio 1
	s_waitcnt lgkmcnt(7)
	v_mfma_f32_16x16x32_bf16 v[60:63], v[142:145], v[174:177], v[60:63]
	v_mfma_f32_16x16x32_bf16 v[56:59], v[150:153], v[174:177], v[56:59]
	s_waitcnt lgkmcnt(5)
	v_mfma_f32_16x16x32_bf16 v[52:55], v[142:145], v[182:185], v[52:55]
	v_mfma_f32_16x16x32_bf16 v[44:47], v[150:153], v[182:185], v[44:47]
	s_waitcnt lgkmcnt(3)
	v_mfma_f32_16x16x32_bf16 v[36:39], v[142:145], v[190:193], v[36:39]
	v_mfma_f32_16x16x32_bf16 v[28:31], v[150:153], v[190:193], v[28:31]
	s_waitcnt lgkmcnt(1)
	v_mfma_f32_16x16x32_bf16 v[20:23], v[142:145], v[198:201], v[20:23]
	v_mfma_f32_16x16x32_bf16 v[12:15], v[150:153], v[198:201], v[12:15]
	v_mfma_f32_16x16x32_bf16 v[60:63], v[146:149], v[178:181], v[60:63]
	v_mfma_f32_16x16x32_bf16 v[56:59], v[154:157], v[178:181], v[56:59]
	v_mfma_f32_16x16x32_bf16 v[52:55], v[146:149], v[186:189], v[52:55]
	v_mfma_f32_16x16x32_bf16 v[44:47], v[154:157], v[186:189], v[44:47]
	v_mfma_f32_16x16x32_bf16 v[36:39], v[146:149], v[194:197], v[36:39]
	v_mfma_f32_16x16x32_bf16 v[28:31], v[154:157], v[194:197], v[28:31]
	s_waitcnt lgkmcnt(0)
	v_mfma_f32_16x16x32_bf16 v[20:23], v[146:149], v[202:205], v[20:23]
	v_mfma_f32_16x16x32_bf16 v[12:15], v[154:157], v[202:205], v[12:15]
	s_setprio 0
	s_setprio 1
	v_mfma_f32_16x16x32_bf16 v[48:51], v[158:161], v[174:177], v[48:51]
	v_mfma_f32_16x16x32_bf16 v[40:43], v[166:169], v[174:177], v[40:43]
	v_mfma_f32_16x16x32_bf16 v[32:35], v[158:161], v[182:185], v[32:35]
	v_mfma_f32_16x16x32_bf16 v[24:27], v[166:169], v[182:185], v[24:27]
	v_mfma_f32_16x16x32_bf16 v[16:19], v[158:161], v[190:193], v[16:19]
	v_mfma_f32_16x16x32_bf16 v[8:11], v[166:169], v[190:193], v[8:11]
	v_mfma_f32_16x16x32_bf16 v[4:7], v[158:161], v[198:201], v[4:7]
	v_mfma_f32_16x16x32_bf16 v[0:3], v[166:169], v[198:201], v[0:3]
	v_mfma_f32_16x16x32_bf16 v[48:51], v[162:165], v[178:181], v[48:51]
	v_mfma_f32_16x16x32_bf16 v[40:43], v[170:173], v[178:181], v[40:43]
	v_mfma_f32_16x16x32_bf16 v[32:35], v[162:165], v[186:189], v[32:35]
	v_mfma_f32_16x16x32_bf16 v[24:27], v[170:173], v[186:189], v[24:27]
	v_mfma_f32_16x16x32_bf16 v[16:19], v[162:165], v[194:197], v[16:19]
	v_mfma_f32_16x16x32_bf16 v[8:11], v[170:173], v[194:197], v[8:11]
	v_mfma_f32_16x16x32_bf16 v[4:7], v[162:165], v[202:205], v[4:7]
	v_mfma_f32_16x16x32_bf16 v[0:3], v[170:173], v[202:205], v[0:3]
	s_setprio 0
	s_barrier
	ds_read_b128 v[142:145], v139
	ds_read_b128 v[146:149], v139 offset:1024
	ds_read_b128 v[150:153], v139 offset:2048
	ds_read_b128 v[154:157], v139 offset:3072
	ds_read_b128 v[158:161], v140
	ds_read_b128 v[162:165], v140 offset:1024
	ds_read_b128 v[166:169], v140 offset:2048
	ds_read_b128 v[170:173], v140 offset:3072
	ds_read_b128 v[174:177], v138 offset:32768
	ds_read_b128 v[178:181], v138 offset:33792
	ds_read_b128 v[182:185], v138 offset:34816
	ds_read_b128 v[186:189], v138 offset:35840
	ds_read_b128 v[190:193], v138 offset:36864
	ds_read_b128 v[194:197], v138 offset:37888
	ds_read_b128 v[198:201], v138 offset:38912
	ds_read_b128 v[202:205], v138 offset:39936
	s_add_u32 s46, s50, 0x40000
	s_addc_u32 s47, s51, 0
	s_mov_b32 s82, m0
	s_mov_b32 m0, s59
	s_nop 0
	global_load_lds_dwordx4 v135, s[46:47]
	s_mov_b32 m0, s82
	s_add_u32 s46, s50, 0x60000
	s_addc_u32 s47, s51, 0
	s_mov_b32 s82, m0
	s_mov_b32 m0, s60
	s_nop 0
	global_load_lds_dwordx4 v135, s[46:47]
	s_mov_b32 m0, s82
	s_waitcnt vmcnt(8)
	s_waitcnt lgkmcnt(0)
	s_barrier
	s_setprio 1
	s_waitcnt lgkmcnt(7)
	v_mfma_f32_16x16x32_bf16 v[124:127], v[142:145], v[174:177], v[124:127]
	v_mfma_f32_16x16x32_bf16 v[120:123], v[150:153], v[174:177], v[120:123]
	s_waitcnt lgkmcnt(5)
	v_mfma_f32_16x16x32_bf16 v[116:119], v[142:145], v[182:185], v[116:119]
	v_mfma_f32_16x16x32_bf16 v[108:111], v[150:153], v[182:185], v[108:111]
	s_waitcnt lgkmcnt(3)
	v_mfma_f32_16x16x32_bf16 v[100:103], v[142:145], v[190:193], v[100:103]
	v_mfma_f32_16x16x32_bf16 v[92:95], v[150:153], v[190:193], v[92:95]
	s_waitcnt lgkmcnt(1)
	v_mfma_f32_16x16x32_bf16 v[84:87], v[142:145], v[198:201], v[84:87]
	v_mfma_f32_16x16x32_bf16 v[76:79], v[150:153], v[198:201], v[76:79]
	v_mfma_f32_16x16x32_bf16 v[124:127], v[146:149], v[178:181], v[124:127]
	v_mfma_f32_16x16x32_bf16 v[120:123], v[154:157], v[178:181], v[120:123]
	v_mfma_f32_16x16x32_bf16 v[116:119], v[146:149], v[186:189], v[116:119]
	v_mfma_f32_16x16x32_bf16 v[108:111], v[154:157], v[186:189], v[108:111]
	v_mfma_f32_16x16x32_bf16 v[100:103], v[146:149], v[194:197], v[100:103]
	v_mfma_f32_16x16x32_bf16 v[92:95], v[154:157], v[194:197], v[92:95]
	s_waitcnt lgkmcnt(0)
	v_mfma_f32_16x16x32_bf16 v[84:87], v[146:149], v[202:205], v[84:87]
	v_mfma_f32_16x16x32_bf16 v[76:79], v[154:157], v[202:205], v[76:79]
	s_setprio 0
	s_setprio 1
	v_mfma_f32_16x16x32_bf16 v[112:115], v[158:161], v[174:177], v[112:115]
	v_mfma_f32_16x16x32_bf16 v[104:107], v[166:169], v[174:177], v[104:107]
	v_mfma_f32_16x16x32_bf16 v[96:99], v[158:161], v[182:185], v[96:99]
	v_mfma_f32_16x16x32_bf16 v[88:91], v[166:169], v[182:185], v[88:91]
	v_mfma_f32_16x16x32_bf16 v[80:83], v[158:161], v[190:193], v[80:83]
	v_mfma_f32_16x16x32_bf16 v[72:75], v[166:169], v[190:193], v[72:75]
	v_mfma_f32_16x16x32_bf16 v[68:71], v[158:161], v[198:201], v[68:71]
	v_mfma_f32_16x16x32_bf16 v[64:67], v[166:169], v[198:201], v[64:67]
	v_mfma_f32_16x16x32_bf16 v[112:115], v[162:165], v[178:181], v[112:115]
	v_mfma_f32_16x16x32_bf16 v[104:107], v[170:173], v[178:181], v[104:107]
	v_mfma_f32_16x16x32_bf16 v[96:99], v[162:165], v[186:189], v[96:99]
	v_mfma_f32_16x16x32_bf16 v[88:91], v[170:173], v[186:189], v[88:91]
	v_mfma_f32_16x16x32_bf16 v[80:83], v[162:165], v[194:197], v[80:83]
	v_mfma_f32_16x16x32_bf16 v[72:75], v[170:173], v[194:197], v[72:75]
	v_mfma_f32_16x16x32_bf16 v[68:71], v[162:165], v[202:205], v[68:71]
	v_mfma_f32_16x16x32_bf16 v[64:67], v[170:173], v[202:205], v[64:67]
	s_setprio 0
	s_barrier
; #define PG8_STAGE_B(bufoff, gbase) PG8_STAGE2S(bufoff, gbase, voffB[0])
; #define PG8_STAGE_A(bufoff, gbase, off, h) do { if constexpr (Sched::GATHERS) PG8_STAGE2(bufoff, gbase, off[h][0], off[h][1]); \
;         else PG8_STAGE2S(bufoff, (const char*)(gbase) + (h) * hstep, voffA0); } while (0)
; #define PG8_LDA(dst, b, h) do { _Pragma("unroll") for (int m = 0; m < 4; ++m) { const v4i_t lo_ = *(const LAS v4i_t*)(lds + PG8_SA(b, h) + aoff + m * 2048), hi_ = *(const LAS v4i_t*)(lds + PG8_SA(b, h) + aoff + m * 2048 + 1024); \
;         dst[m] = __builtin_shufflevector(lo_, hi_, 0, 1, 2, 3, 4, 5, 6, 7); } } while (0)
; #define PG8_WAIT_V(n) asm volatile("s_waitcnt vmcnt(" #n ")" ::: "memory")
; #define PG8_WAIT_L(n) asm volatile("s_waitcnt lgkmcnt(" #n ")" ::: "memory")
; #define PG8_BAR __builtin_amdgcn_s_barrier()
; #define PG8_SCHED __builtin_amdgcn_sched_barrier(0)
; template <class Epi, class Sched>
; __device__ __forceinline__ void gemm_phase(LAS unsigned char* lds, const Sched& S, const Epi& E, const int wid) {
;     ...
;             PG8_LDA(At, 1, 1); PG8_STAGE_B(PG8_SB(1, 0), b3); PG8_STAGE_B(PG8_SB(1, 1), b3 + hstep); PG8_STAGE_A(PG8_SA(1, 0), a3, o2, 0);
;             PG8_WAIT_V(8); PG8_WAIT_L(0); PG8_BAR; PG8_MMA(1, 0, At, B0); PG8_MMA(1, 1, At, B1); PG8_BAR; PG8_SCHED;
;         }
;         if (wr == 0) PG8_BAR;
	s_add_u32 s46, s54, 0x80
	s_addc_u32 s47, s55, 0
	ds_read_b128 v[174:177], v138 offset:49152
	ds_read_b128 v[178:181], v138 offset:50176
	ds_read_b128 v[182:185], v138 offset:51200
	ds_read_b128 v[186:189], v138 offset:52224
	ds_read_b128 v[190:193], v138 offset:53248
	ds_read_b128 v[194:197], v138 offset:54272
	ds_read_b128 v[198:201], v138 offset:55296
	ds_read_b128 v[202:205], v138 offset:56320
	s_mov_b32 s82, m0
	s_mov_b32 m0, s63
	s_nop 0
	global_load_lds_dwordx4 v134, s[46:47]
	s_mov_b32 m0, s82
	s_add_u32 s46, s54, 0x20080
	s_addc_u32 s47, s55, 0
	s_mov_b32 s82, m0
	s_mov_b32 m0, s64
	s_nop 0
	global_load_lds_dwordx4 v134, s[46:47]
	s_mov_b32 m0, s82
	s_add_u32 s46, s54, 0x40080
	s_addc_u32 s47, s55, 0
	s_mov_b32 s82, m0
	s_mov_b32 m0, s67
	s_nop 0
	global_load_lds_dwordx4 v134, s[46:47]
	s_mov_b32 m0, s82
	s_add_u32 s46, s54, 0x60080
	s_addc_u32 s47, s55, 0
	s_mov_b32 s54, m0
	s_mov_b32 m0, s68
	s_nop 0
	global_load_lds_dwordx4 v134, s[46:47]
	s_mov_b32 m0, s54
	s_mov_b32 s46, m0
	s_mov_b32 m0, s65
	s_nop 0
	global_load_lds_dwordx4 v135, s[52:53]
	s_mov_b32 m0, s46
	s_add_u32 s46, s50, 0x20080
	s_addc_u32 s47, s51, 0
	s_mov_b32 s50, m0
	s_mov_b32 m0, s66
	s_nop 0
	global_load_lds_dwordx4 v135, s[46:47]
	s_mov_b32 m0, s50
	s_waitcnt vmcnt(8)
	s_waitcnt lgkmcnt(0)
	s_barrier
	s_setprio 1
	s_waitcnt lgkmcnt(7)
	v_mfma_f32_16x16x32_bf16 v[60:63], v[142:145], v[174:177], v[60:63]
	v_mfma_f32_16x16x32_bf16 v[56:59], v[150:153], v[174:177], v[56:59]
	s_waitcnt lgkmcnt(5)
	v_mfma_f32_16x16x32_bf16 v[52:55], v[142:145], v[182:185], v[52:55]
	v_mfma_f32_16x16x32_bf16 v[44:47], v[150:153], v[182:185], v[44:47]
	s_waitcnt lgkmcnt(3)
	v_mfma_f32_16x16x32_bf16 v[36:39], v[142:145], v[190:193], v[36:39]
	v_mfma_f32_16x16x32_bf16 v[28:31], v[150:153], v[190:193], v[28:31]
	s_waitcnt lgkmcnt(1)
	v_mfma_f32_16x16x32_bf16 v[20:23], v[142:145], v[198:201], v[20:23]
	v_mfma_f32_16x16x32_bf16 v[12:15], v[150:153], v[198:201], v[12:15]
	v_mfma_f32_16x16x32_bf16 v[60:63], v[146:149], v[178:181], v[60:63]
	v_mfma_f32_16x16x32_bf16 v[56:59], v[154:157], v[178:181], v[56:59]
	v_mfma_f32_16x16x32_bf16 v[52:55], v[146:149], v[186:189], v[52:55]
	v_mfma_f32_16x16x32_bf16 v[44:47], v[154:157], v[186:189], v[44:47]
	v_mfma_f32_16x16x32_bf16 v[36:39], v[146:149], v[194:197], v[36:39]
	v_mfma_f32_16x16x32_bf16 v[28:31], v[154:157], v[194:197], v[28:31]
	s_waitcnt lgkmcnt(0)
	v_mfma_f32_16x16x32_bf16 v[20:23], v[146:149], v[202:205], v[20:23]
	v_mfma_f32_16x16x32_bf16 v[12:15], v[154:157], v[202:205], v[12:15]
	s_setprio 0
	s_setprio 1
	v_mfma_f32_16x16x32_bf16 v[48:51], v[158:161], v[174:177], v[48:51]
	v_mfma_f32_16x16x32_bf16 v[40:43], v[166:169], v[174:177], v[40:43]
	v_mfma_f32_16x16x32_bf16 v[32:35], v[158:161], v[182:185], v[32:35]
	v_mfma_f32_16x16x32_bf16 v[24:27], v[166:169], v[182:185], v[24:27]
	v_mfma_f32_16x16x32_bf16 v[16:19], v[158:161], v[190:193], v[16:19]
	v_mfma_f32_16x16x32_bf16 v[8:11], v[166:169], v[190:193], v[8:11]
	v_mfma_f32_16x16x32_bf16 v[4:7], v[158:161], v[198:201], v[4:7]
	v_mfma_f32_16x16x32_bf16 v[0:3], v[166:169], v[198:201], v[0:3]
	v_mfma_f32_16x16x32_bf16 v[48:51], v[162:165], v[178:181], v[48:51]
	v_mfma_f32_16x16x32_bf16 v[40:43], v[170:173], v[178:181], v[40:43]
	v_mfma_f32_16x16x32_bf16 v[32:35], v[162:165], v[186:189], v[32:35]
	v_mfma_f32_16x16x32_bf16 v[24:27], v[170:173], v[186:189], v[24:27]
	v_mfma_f32_16x16x32_bf16 v[16:19], v[162:165], v[194:197], v[16:19]
	v_mfma_f32_16x16x32_bf16 v[8:11], v[170:173], v[194:197], v[8:11]
	v_mfma_f32_16x16x32_bf16 v[4:7], v[162:165], v[202:205], v[4:7]
	v_mfma_f32_16x16x32_bf16 v[0:3], v[170:173], v[202:205], v[0:3]
	s_setprio 0
	s_barrier
	s_add_i32 s81, s81, 2
	s_add_u32 s79, s79, 0x100
	s_addc_u32 s80, s80, 0
	s_cmp_gt_u32 s81, 13
	s_mov_b64 s[46:47], s[48:49]
	s_cbranch_scc0 .LBB7_627
	s_mov_b32 s99, 1
	s_and_b64 vcc, exec, s[8:9]
	s_cbranch_vccz .LBB7_630
	s_barrier
